# speedup vs baseline: 1.0138x; 1.0138x over previous
.LBB1_93:
	s_waitcnt vmcnt(0)
	v_mfma_scale_f32_32x32x64_f8f6f4 v[2:17], v[58:65], v[98:105], v[2:17], v201, v201 op_sel_hi:[0,0,0]
	v_lshlrev_b32_e32 v18, 7, v196
	s_waitcnt lgkmcnt(0)
	s_barrier
	ds_read_b128 v[162:165], v18 offset:37376
	ds_read_b128 v[166:169], v18 offset:37392
	ds_read_b128 v[170:173], v18 offset:37408
	ds_read_b128 v[174:177], v18 offset:37424
	ds_read_b128 v[178:181], v18 offset:37440
	ds_read_b128 v[182:185], v18 offset:37456
	ds_read_b128 v[186:189], v18 offset:37472
	ds_read_b128 v[190:193], v18 offset:37488
	s_lshl_b32 s34, s35, 3
	v_or_b32_e32 v202, 0x9100, v18
	s_add_i32 s38, s34, 16
	v_mov_b32_e32 v201, 0
	s_mov_b32 s39, -2
	v_mov_b32_e32 v203, 0x7f7f7f7f
	v_mov_b32_e32 v0, 0
	v_mov_b32_e32 v1, 0
	s_mov_b32 s39, 0

.Lq2_nd0_3:
	v_mfma_scale_f32_32x32x64_f8f6f4 v[18:33], v[66:73], v[146:153], 0, v203, v203 op_sel_hi:[0,0,0]
	ds_read_b128 v[236:239], v202
	v_exp_f32_e64 v2, -v2
	v_exp_f32_e64 v3, -v3
	v_exp_f32_e64 v4, -v4
	v_exp_f32_e64 v5, -v5
	s_waitcnt lgkmcnt(1)
	v_add_co_u32_e64 v200, s[42:43], v200, v200
	v_add_co_u32_e64 v200, s[48:49], v200, v200
	v_add_co_u32_e64 v200, s[50:51], v200, v200
	v_add_co_u32_e64 v200, s[56:57], v200, v200
	v_pk_add_f32 v[2:3], v[2:3], v[162:163]
	v_pk_add_f32 v[4:5], v[4:5], v[164:165]
	s_mov_b64 exec, s[42:43]
	v_mul_f32_e32 v204, v204, v2
	s_mov_b64 exec, s[48:49]
	v_mul_f32_e32 v205, v205, v3
	s_mov_b64 exec, s[50:51]
	v_mul_f32_e32 v206, v206, v4
	s_mov_b64 exec, s[56:57]
	v_mul_f32_e32 v207, v207, v5
	s_mov_b64 exec, -1
	s_nop 1
	v_log_f32_e32 v2, v204
	v_log_f32_e32 v3, v205
	v_log_f32_e32 v4, v206
	v_log_f32_e32 v5, v207
	s_waitcnt lgkmcnt(0)
	v_pk_fma_f32 v[0:1], v[2:3], v[236:237], v[0:1]
	v_pk_fma_f32 v[0:1], v[4:5], v[238:239], v[0:1]
	v_mfma_scale_f32_32x32x64_f8f6f4 v[18:33], v[74:81], v[154:161], v[18:33], v203, v203 op_sel_hi:[0,0,0]
	ds_read_b128 v[236:239], v202 offset:16
	v_exp_f32_e64 v6, -v6
	v_exp_f32_e64 v7, -v7
	v_exp_f32_e64 v8, -v8
	v_exp_f32_e64 v9, -v9
	v_add_co_u32_e64 v200, s[42:43], v200, v200
	v_add_co_u32_e64 v200, s[48:49], v200, v200
	v_add_co_u32_e64 v200, s[50:51], v200, v200
	v_add_co_u32_e64 v200, s[56:57], v200, v200
	v_pk_add_f32 v[6:7], v[6:7], v[166:167]
	v_pk_add_f32 v[8:9], v[8:9], v[168:169]
	s_mov_b64 exec, s[42:43]
	v_mul_f32_e32 v208, v208, v6
	s_mov_b64 exec, s[48:49]
	v_mul_f32_e32 v209, v209, v7
	s_mov_b64 exec, s[50:51]
	v_mul_f32_e32 v210, v210, v8
	s_mov_b64 exec, s[56:57]
	v_mul_f32_e32 v211, v211, v9
	s_mov_b64 exec, -1
	s_nop 1
	v_log_f32_e32 v6, v208
	v_log_f32_e32 v7, v209
	v_log_f32_e32 v8, v210
	v_log_f32_e32 v9, v211
	s_waitcnt lgkmcnt(0)
	v_pk_fma_f32 v[0:1], v[6:7], v[236:237], v[0:1]
	v_pk_fma_f32 v[0:1], v[8:9], v[238:239], v[0:1]
	v_mfma_scale_f32_32x32x64_f8f6f4 v[18:33], v[82:89], v[138:145], v[18:33], v203, v203 op_sel_hi:[0,0,0]
	ds_read_b128 v[236:239], v202 offset:32
	v_exp_f32_e64 v10, -v10
	v_exp_f32_e64 v11, -v11
	v_exp_f32_e64 v12, -v12
	v_exp_f32_e64 v13, -v13
	v_add_co_u32_e64 v200, s[42:43], v200, v200
	v_add_co_u32_e64 v200, s[48:49], v200, v200
	v_add_co_u32_e64 v200, s[50:51], v200, v200
	v_add_co_u32_e64 v200, s[56:57], v200, v200
	v_pk_add_f32 v[10:11], v[10:11], v[170:171]
	v_pk_add_f32 v[12:13], v[12:13], v[172:173]
	s_mov_b64 exec, s[42:43]
	v_mul_f32_e32 v212, v212, v10
	s_mov_b64 exec, s[48:49]
	v_mul_f32_e32 v213, v213, v11
	s_mov_b64 exec, s[50:51]
	v_mul_f32_e32 v214, v214, v12
	s_mov_b64 exec, s[56:57]
	v_mul_f32_e32 v215, v215, v13
	s_mov_b64 exec, -1
	s_nop 1
	v_log_f32_e32 v10, v212
	v_log_f32_e32 v11, v213
	v_log_f32_e32 v12, v214
	v_log_f32_e32 v13, v215
	s_waitcnt lgkmcnt(0)
	v_pk_fma_f32 v[0:1], v[10:11], v[236:237], v[0:1]
	v_pk_fma_f32 v[0:1], v[12:13], v[238:239], v[0:1]
	v_mfma_scale_f32_32x32x64_f8f6f4 v[18:33], v[90:97], v[130:137], v[18:33], v203, v203 op_sel_hi:[0,0,0]
	ds_read_b128 v[236:239], v202 offset:48
	v_exp_f32_e64 v14, -v14
	v_exp_f32_e64 v15, -v15
	v_exp_f32_e64 v16, -v16
	v_exp_f32_e64 v17, -v17
	v_add_co_u32_e64 v200, s[42:43], v200, v200
	v_add_co_u32_e64 v200, s[48:49], v200, v200
	v_add_co_u32_e64 v200, s[50:51], v200, v200
	v_add_co_u32_e64 v200, s[56:57], v200, v200
	v_pk_add_f32 v[14:15], v[14:15], v[174:175]
	v_pk_add_f32 v[16:17], v[16:17], v[176:177]
	s_mov_b64 exec, s[42:43]
	v_mul_f32_e32 v216, v216, v14
	s_mov_b64 exec, s[48:49]
	v_mul_f32_e32 v217, v217, v15
	s_mov_b64 exec, s[50:51]
	v_mul_f32_e32 v218, v218, v16
	s_mov_b64 exec, s[56:57]
	v_mul_f32_e32 v219, v219, v17
	s_mov_b64 exec, -1
	s_nop 1
	v_log_f32_e32 v14, v216
	v_log_f32_e32 v15, v217
	v_log_f32_e32 v16, v218
	v_log_f32_e32 v17, v219
	s_waitcnt lgkmcnt(0)
	v_pk_fma_f32 v[0:1], v[14:15], v[236:237], v[0:1]
	v_pk_fma_f32 v[0:1], v[16:17], v[238:239], v[0:1]
	s_cmp_lg_u32 s55, s40
	s_cbranch_scc1 .Lq2_nd1_3
	s_nop 15
	s_nop 7
	v_cndmask_b32_e64 v18, v18, v199, s[0:1]
	v_cndmask_b32_e64 v19, v19, v199, s[2:3]
	v_cndmask_b32_e64 v20, v20, v199, s[4:5]
	v_cndmask_b32_e64 v21, v21, v199, s[6:7]
	v_cndmask_b32_e64 v22, v22, v199, s[8:9]
	v_cndmask_b32_e64 v23, v23, v199, s[10:11]
	v_cndmask_b32_e64 v24, v24, v199, s[12:13]
	v_cndmask_b32_e64 v25, v25, v199, s[14:15]
	v_cndmask_b32_e64 v26, v26, v199, s[16:17]
	v_cndmask_b32_e64 v27, v27, v199, s[18:19]
	v_cndmask_b32_e64 v28, v28, v199, s[20:21]
	v_cndmask_b32_e64 v29, v29, v199, s[22:23]
	v_cndmask_b32_e64 v30, v30, v199, s[24:25]
	v_cndmask_b32_e64 v31, v31, v199, s[26:27]
	v_cndmask_b32_e64 v32, v32, v199, s[28:29]
	v_cndmask_b32_e64 v33, v33, v199, s[30:31]
.Lq2_nd1_3:
	s_nop 3
	s_waitcnt vmcnt(6)
	v_mfma_scale_f32_32x32x64_f8f6f4 v[2:17], v[34:41], v[106:113], 0, v203, v203 op_sel_hi:[0,0,0]
	ds_read_b128 v[236:239], v202 offset:64
	v_exp_f32_e64 v18, -v18
	v_exp_f32_e64 v19, -v19
	v_exp_f32_e64 v20, -v20
	v_exp_f32_e64 v21, -v21
	v_add_co_u32_e64 v200, s[42:43], v200, v200
	v_add_co_u32_e64 v200, s[48:49], v200, v200
	v_add_co_u32_e64 v200, s[50:51], v200, v200
	v_add_co_u32_e64 v200, s[56:57], v200, v200
	v_pk_add_f32 v[18:19], v[18:19], v[178:179]
	v_pk_add_f32 v[20:21], v[20:21], v[180:181]
	s_mov_b64 exec, s[42:43]
	v_mul_f32_e32 v220, v220, v18
	s_mov_b64 exec, s[48:49]
	v_mul_f32_e32 v221, v221, v19
	s_mov_b64 exec, s[50:51]
	v_mul_f32_e32 v222, v222, v20
	s_mov_b64 exec, s[56:57]
	v_mul_f32_e32 v223, v223, v21
	s_mov_b64 exec, -1
	s_nop 1
	v_log_f32_e32 v18, v220
	v_log_f32_e32 v19, v221
	v_log_f32_e32 v20, v222
	v_log_f32_e32 v21, v223
	s_waitcnt lgkmcnt(0)
	v_pk_fma_f32 v[0:1], v[18:19], v[236:237], v[0:1]
	v_pk_fma_f32 v[0:1], v[20:21], v[238:239], v[0:1]
	s_waitcnt vmcnt(4)
	v_mfma_scale_f32_32x32x64_f8f6f4 v[2:17], v[42:49], v[122:129], v[2:17], v203, v203 op_sel_hi:[0,0,0]
	ds_read_b128 v[236:239], v202 offset:80
	v_exp_f32_e64 v22, -v22
	v_exp_f32_e64 v23, -v23
	v_exp_f32_e64 v24, -v24
	v_exp_f32_e64 v25, -v25
	v_add_co_u32_e64 v200, s[42:43], v200, v200
	v_add_co_u32_e64 v200, s[48:49], v200, v200
	v_add_co_u32_e64 v200, s[50:51], v200, v200
	v_add_co_u32_e64 v200, s[56:57], v200, v200
	v_pk_add_f32 v[22:23], v[22:23], v[182:183]
	v_pk_add_f32 v[24:25], v[24:25], v[184:185]
	s_mov_b64 exec, s[42:43]
	v_mul_f32_e32 v224, v224, v22
	s_mov_b64 exec, s[48:49]
	v_mul_f32_e32 v225, v225, v23
	s_mov_b64 exec, s[50:51]
	v_mul_f32_e32 v226, v226, v24
	s_mov_b64 exec, s[56:57]
	v_mul_f32_e32 v227, v227, v25
	s_mov_b64 exec, -1
	s_nop 1
	v_log_f32_e32 v22, v224
	v_log_f32_e32 v23, v225
	v_log_f32_e32 v24, v226
	v_log_f32_e32 v25, v227
	s_waitcnt lgkmcnt(0)
	v_pk_fma_f32 v[0:1], v[22:23], v[236:237], v[0:1]
	v_pk_fma_f32 v[0:1], v[24:25], v[238:239], v[0:1]
	s_waitcnt vmcnt(2)
	v_mfma_scale_f32_32x32x64_f8f6f4 v[2:17], v[50:57], v[114:121], v[2:17], v203, v203 op_sel_hi:[0,0,0]
	ds_read_b128 v[236:239], v202 offset:96
	v_exp_f32_e64 v26, -v26
	v_exp_f32_e64 v27, -v27
	v_exp_f32_e64 v28, -v28
	v_exp_f32_e64 v29, -v29
	v_add_co_u32_e64 v200, s[42:43], v200, v200
	v_add_co_u32_e64 v200, s[48:49], v200, v200
	v_add_co_u32_e64 v200, s[50:51], v200, v200
	v_add_co_u32_e64 v200, s[56:57], v200, v200
	v_pk_add_f32 v[26:27], v[26:27], v[186:187]
	v_pk_add_f32 v[28:29], v[28:29], v[188:189]
	s_mov_b64 exec, s[42:43]
	v_mul_f32_e32 v228, v228, v26
	s_mov_b64 exec, s[48:49]
	v_mul_f32_e32 v229, v229, v27
	s_mov_b64 exec, s[50:51]
	v_mul_f32_e32 v230, v230, v28
	s_mov_b64 exec, s[56:57]
	v_mul_f32_e32 v231, v231, v29
	s_mov_b64 exec, -1
	s_nop 1
	v_log_f32_e32 v26, v228
	v_log_f32_e32 v27, v229
	v_log_f32_e32 v28, v230
	v_log_f32_e32 v29, v231
	s_waitcnt lgkmcnt(0)
	v_pk_fma_f32 v[0:1], v[26:27], v[236:237], v[0:1]
	v_pk_fma_f32 v[0:1], v[28:29], v[238:239], v[0:1]
	s_waitcnt vmcnt(0)
	v_mfma_scale_f32_32x32x64_f8f6f4 v[2:17], v[58:65], v[98:105], v[2:17], v203, v203 op_sel_hi:[0,0,0]
	ds_read_b128 v[236:239], v202 offset:112
	v_exp_f32_e64 v30, -v30
	v_exp_f32_e64 v31, -v31
	v_exp_f32_e64 v32, -v32
	v_exp_f32_e64 v33, -v33
	v_add_co_u32_e64 v200, s[42:43], v200, v200
	v_add_co_u32_e64 v200, s[48:49], v200, v200
	v_add_co_u32_e64 v200, s[50:51], v200, v200
	v_add_co_u32_e64 v200, s[56:57], v200, v200
	v_pk_add_f32 v[30:31], v[30:31], v[190:191]
	v_pk_add_f32 v[32:33], v[32:33], v[192:193]
	s_mov_b64 exec, s[42:43]
	v_mul_f32_e32 v232, v232, v30
	s_mov_b64 exec, s[48:49]
	v_mul_f32_e32 v233, v233, v31
	s_mov_b64 exec, s[50:51]
	v_mul_f32_e32 v234, v234, v32
	s_mov_b64 exec, s[56:57]
	v_mul_f32_e32 v235, v235, v33
	s_mov_b64 exec, -1
	s_nop 1
	v_log_f32_e32 v30, v232
	v_log_f32_e32 v31, v233
	v_log_f32_e32 v32, v234
	v_log_f32_e32 v33, v235
	s_waitcnt lgkmcnt(0)
	v_pk_fma_f32 v[0:1], v[30:31], v[236:237], v[0:1]
	v_pk_fma_f32 v[0:1], v[32:33], v[238:239], v[0:1]
	s_add_i32 s39, s39, 1
	s_cmp_lt_u32 s39, 4
	s_cbranch_scc1 .Lq2_loop
	v_add_f32_e32 v201, v0, v1
